# P9: per-row-group slot bases from one returning global atomic on the expert counters (no all-row-group count table), P8->P9 grid barrier removed
# baseline (speedup 1.0000x reference)
.LBB0_845:
	v_readlane_b32 s0, v243, 0
	v_readlane_b32 s2, v243, 2
	v_readlane_b32 s3, v243, 3
	v_readlane_b32 s1, v243, 1
	s_cmp_gt_i32 s3, 9
	v_readlane_b32 s2, v243, 20
	s_cselect_b64 s[0:1], -1, 0
	v_readlane_b32 s3, v243, 21
	s_and_b64 s[2:3], s[2:3], s[0:1]
	s_andn2_b64 vcc, exec, s[2:3]
	s_branch .LBB0_899
	s_waitcnt vmcnt(0)
	s_barrier
	s_mov_b64 s[2:3], exec
	v_readlane_b32 s4, v243, 10
	v_readlane_b32 s5, v243, 11
	s_and_b64 s[4:5], s[2:3], s[4:5]
	s_mov_b64 exec, s[4:5]
	s_cbranch_execz .LBB0_898
	s_add_i32 s4, 0, 0x20000
	v_mov_b32_e32 v1, s4
	s_waitcnt vmcnt(0) expcnt(0) lgkmcnt(0)
	buffer_inv sc1
	ds_read_b32 v3, v1
	s_add_i32 s4, 0, 0x20004
	v_mov_b32_e32 v1, s4
	ds_read_b32 v1, v1
	s_waitcnt lgkmcnt(1)
	v_cmp_ne_u32_e32 vcc, 0, v3
	s_cbranch_vccnz .LBB0_862
	v_readlane_b32 s4, v243, 4
	v_readlane_b32 s5, v243, 5
	s_load_dwordx2 s[8:9], s[4:5], 0x4
	v_readlane_b32 s40, v243, 0
	v_readlane_b32 s41, v243, 1
	s_add_u32 s4, s40, 0x4200
	s_addc_u32 s5, s41, 0
	s_add_u32 s6, s40, 0x4400
	s_addc_u32 s7, s41, 0
	s_waitcnt lgkmcnt(0)
	s_mul_i32 s46, s8, s33
	s_add_u32 s8, s40, 0x4500
	s_mul_i32 s46, s46, s9
	s_addc_u32 s9, s41, 0
	s_add_u32 s10, s40, 0x4600
	s_addc_u32 s11, s41, 0
	s_add_u32 s12, s40, 0x4700
	s_addc_u32 s13, s41, 0
	s_add_u32 s14, s40, 0x4800
	s_addc_u32 s15, s41, 0
	s_add_u32 s16, s40, 0x4900
	s_addc_u32 s17, s41, 0
	s_add_u32 s18, s40, 0x4a00
	s_addc_u32 s19, s41, 0
	s_add_u32 s20, s40, 0x4b00
	s_addc_u32 s21, s41, 0
	s_add_u32 s22, s40, 0x4c00
	s_addc_u32 s23, s41, 0
	s_add_u32 s24, s40, 0x4d00
	s_addc_u32 s25, s41, 0
	s_add_u32 s26, s40, 0x4e00
	s_addc_u32 s27, s41, 0
	s_add_u32 s28, s40, 0x4f00
	s_addc_u32 s29, s41, 0
	s_add_u32 s30, s40, 0x5000
	s_addc_u32 s31, s41, 0
	s_add_u32 s34, s40, 0x5100
	s_addc_u32 s35, s41, 0
	s_add_u32 s36, s40, 0x5200
	s_addc_u32 s37, s41, 0
	s_add_u32 s38, s40, 0x5300
	s_addc_u32 s39, s41, 0
	s_mov_b32 s47, 1
	v_mov_b32_e32 v17, 0
	v_readlane_b32 s42, v243, 2
	v_readlane_b32 s43, v243, 3
	s_branch .LBB0_850

.LBB0_903:
	s_waitcnt vmcnt(0)
	s_and_saveexec_b64 s[2:3], vcc
	v_readlane_b32 s56, v243, 18
	v_readlane_b32 s57, v243, 19
	s_cbranch_execz .LBB0_908
	ds_read_b32 v2, v21 offset:512
	s_waitcnt lgkmcnt(0)
	global_atomic_add v3, v[26:27], v2, off offset:256 sc0
	s_waitcnt vmcnt(0)
	ds_write_b32 v30, v3 offset:8192
